# P6 out-proj epilogue: one-dword touch loads of the later residual rows issued with the first batch so later drains hit L2, on top of v5_ffta
# speedup vs baseline: 1.0046x; 1.0000x over previous
.LBB0_1324:
	s_add_u32 s14, s46, s12
	s_addc_u32 s15, s47, s13
	s_add_u32 s26, s14, 0x1701b100
	s_addc_u32 s27, s15, 0
	s_add_u32 s36, s3, s12
	s_addc_u32 s40, s24, s13
	s_add_i32 s41, 0, 0x10000
	v_add_u32_e32 v37, s41, v175
	ds_read_b128 v[48:51], v37
	ds_read_b128 v[184:187], v37 offset:1024
	ds_read_b128 v[188:191], v37 offset:2048
	ds_read_b128 v[192:195], v37 offset:3072
	s_cmpk_eq_i32 s12, 0x700
	s_cselect_b64 vcc, -1, 0
	s_and_b64 s[14:15], vcc, exec
	v_cndmask_b32_e32 v2, v36, v177, vcc
	s_cselect_b32 s35, s49, s27
	s_cselect_b32 s34, s48, s26
	v_cndmask_b32_e32 v170, v38, v178, vcc
	v_cndmask_b32_e32 v37, v40, v179, vcc
	v_cndmask_b32_e32 v39, v42, v182, vcc
	s_cselect_b32 s15, s0, s40
	s_cselect_b32 s14, s1, s36
	v_lshl_add_u64 v[234:235], v[46:47], 0, s[12:13]
	s_add_i32 m0, s62, 0xc000
	ds_read_b128 v[196:199], v176
	ds_read_b128 v[200:203], v176 offset:1024
	ds_read_b128 v[204:207], v176 offset:2048
	ds_read_b128 v[214:217], v176 offset:3072
	ds_read_b128 v[218:221], v176 offset:4096
	ds_read_b128 v[222:225], v176 offset:5120
	ds_read_b128 v[226:229], v176 offset:6144
	ds_read_b128 v[230:233], v176 offset:7168
	global_load_lds_dwordx4 v[234:235], off
	v_lshl_add_u64 v[234:235], v[44:45], 0, s[12:13]
	s_add_i32 m0, s62, 0xe000
	s_nop 0
	global_load_lds_dwordx4 v[234:235], off
	s_waitcnt lgkmcnt(8)
	s_barrier
	s_waitcnt lgkmcnt(0)
	s_setprio 1
	s_waitcnt lgkmcnt(0)
	v_mfma_f32_16x16x32_bf16 v[144:147], v[48:51], v[196:199], v[144:147]
	v_mfma_f32_16x16x32_bf16 v[140:143], v[188:191], v[196:199], v[140:143]
	v_mfma_f32_16x16x32_bf16 v[136:139], v[48:51], v[204:207], v[136:139]
	v_mfma_f32_16x16x32_bf16 v[132:135], v[188:191], v[204:207], v[132:135]
	v_mfma_f32_16x16x32_bf16 v[112:115], v[48:51], v[218:221], v[112:115]
	v_mfma_f32_16x16x32_bf16 v[108:111], v[188:191], v[218:221], v[108:111]
	v_mfma_f32_16x16x32_bf16 v[104:107], v[48:51], v[226:229], v[104:107]
	v_mfma_f32_16x16x32_bf16 v[100:103], v[188:191], v[226:229], v[100:103]
	v_mfma_f32_16x16x32_bf16 v[144:147], v[184:187], v[200:203], v[144:147]
	v_mfma_f32_16x16x32_bf16 v[140:143], v[192:195], v[200:203], v[140:143]
	v_mfma_f32_16x16x32_bf16 v[136:139], v[184:187], v[214:217], v[136:139]
	v_mfma_f32_16x16x32_bf16 v[132:135], v[192:195], v[214:217], v[132:135]
	v_mfma_f32_16x16x32_bf16 v[112:115], v[184:187], v[222:225], v[112:115]
	v_mfma_f32_16x16x32_bf16 v[108:111], v[192:195], v[222:225], v[108:111]
	v_mfma_f32_16x16x32_bf16 v[104:107], v[184:187], v[230:233], v[104:107]
	v_mfma_f32_16x16x32_bf16 v[100:103], v[192:195], v[230:233], v[100:103]
	s_setprio 0
	s_barrier
	s_add_i32 s36, 0, 0x14000
	s_add_i32 s26, s41, s61
	v_add_u32_e32 v41, s36, v175
	v_lshl_add_u64 v[250:251], s[14:15], 0, v[148:149]
	s_mov_b32 m0, s26
	ds_read_b128 v[234:237], v41
	ds_read_b128 v[238:241], v41 offset:1024
	ds_read_b128 v[242:245], v41 offset:2048
	ds_read_b128 v[246:249], v41 offset:3072
	global_load_lds_dwordx4 v[250:251], off
	v_lshl_add_u64 v[252:253], s[14:15], 0, v[150:151]
	s_add_i32 m0, s26, 0x2000
	s_nop 0
	global_load_lds_dwordx4 v[252:253], off
	s_barrier
	s_waitcnt lgkmcnt(0)
	s_setprio 1
	s_waitcnt lgkmcnt(0)
	v_mfma_f32_16x16x32_bf16 v[128:131], v[234:237], v[196:199], v[128:131]
	v_mfma_f32_16x16x32_bf16 v[124:127], v[242:245], v[196:199], v[124:127]
	v_mfma_f32_16x16x32_bf16 v[120:123], v[234:237], v[204:207], v[120:123]
	v_mfma_f32_16x16x32_bf16 v[116:119], v[242:245], v[204:207], v[116:119]
	v_mfma_f32_16x16x32_bf16 v[96:99], v[234:237], v[218:221], v[96:99]
	v_mfma_f32_16x16x32_bf16 v[92:95], v[242:245], v[218:221], v[92:95]
	v_mfma_f32_16x16x32_bf16 v[88:91], v[234:237], v[226:229], v[88:91]
	v_mfma_f32_16x16x32_bf16 v[84:87], v[242:245], v[226:229], v[84:87]
	v_mfma_f32_16x16x32_bf16 v[128:131], v[238:241], v[200:203], v[128:131]
	v_mfma_f32_16x16x32_bf16 v[124:127], v[246:249], v[200:203], v[124:127]
	v_mfma_f32_16x16x32_bf16 v[120:123], v[238:241], v[214:217], v[120:123]
	v_mfma_f32_16x16x32_bf16 v[116:119], v[246:249], v[214:217], v[116:119]
	v_mfma_f32_16x16x32_bf16 v[96:99], v[238:241], v[222:225], v[96:99]
	v_mfma_f32_16x16x32_bf16 v[92:95], v[246:249], v[222:225], v[92:95]
	v_mfma_f32_16x16x32_bf16 v[88:91], v[238:241], v[230:233], v[88:91]
	v_mfma_f32_16x16x32_bf16 v[84:87], v[246:249], v[230:233], v[84:87]
	s_setprio 0
	s_mov_b32 m0, s62
	s_barrier
	ds_read_b128 v[196:199], v176 offset:16384
	ds_read_b128 v[200:203], v176 offset:17408
	ds_read_b128 v[204:207], v176 offset:18432
	ds_read_b128 v[214:217], v176 offset:19456
	ds_read_b128 v[218:221], v176 offset:20480
	ds_read_b128 v[222:225], v176 offset:21504
	ds_read_b128 v[226:229], v176 offset:22528
	ds_read_b128 v[230:233], v176 offset:23552
	global_load_lds_dwordx4 v2, s[34:35]
	s_mov_b32 m0, s63
	v_mov_b32_e32 v171, v3
	global_load_lds_dwordx4 v170, s[34:35]
	s_barrier
	s_waitcnt lgkmcnt(0)
	v_lshl_add_u64 v[208:209], s[34:35], 0, v[2:3]
	v_lshl_add_u64 v[170:171], s[34:35], 0, v[170:171]
	s_setprio 1
	s_waitcnt lgkmcnt(0)
	v_mfma_f32_16x16x32_bf16 v[80:83], v[48:51], v[196:199], v[80:83]
	v_mfma_f32_16x16x32_bf16 v[76:79], v[188:191], v[196:199], v[76:79]
	v_mfma_f32_16x16x32_bf16 v[72:75], v[48:51], v[204:207], v[72:75]
	v_mfma_f32_16x16x32_bf16 v[68:71], v[188:191], v[204:207], v[68:71]
	v_mfma_f32_16x16x32_bf16 v[16:19], v[48:51], v[218:221], v[16:19]
	v_mfma_f32_16x16x32_bf16 v[12:15], v[188:191], v[218:221], v[12:15]
	v_mfma_f32_16x16x32_bf16 v[8:11], v[48:51], v[226:229], v[8:11]
	v_mfma_f32_16x16x32_bf16 v[4:7], v[188:191], v[226:229], v[4:7]
	v_mfma_f32_16x16x32_bf16 v[80:83], v[184:187], v[200:203], v[80:83]
	v_mfma_f32_16x16x32_bf16 v[76:79], v[192:195], v[200:203], v[76:79]
	v_mfma_f32_16x16x32_bf16 v[72:75], v[184:187], v[214:217], v[72:75]
	v_mfma_f32_16x16x32_bf16 v[68:71], v[192:195], v[214:217], v[68:71]
	v_mfma_f32_16x16x32_bf16 v[16:19], v[184:187], v[222:225], v[16:19]
	v_mfma_f32_16x16x32_bf16 v[12:15], v[192:195], v[222:225], v[12:15]
	v_mfma_f32_16x16x32_bf16 v[8:11], v[184:187], v[230:233], v[8:11]
	v_mfma_f32_16x16x32_bf16 v[4:7], v[192:195], v[230:233], v[4:7]
	s_setprio 0
	s_barrier
	s_add_u32 s26, s14, 0x40000
	s_addc_u32 s27, s15, 0
	s_add_i32 s36, s36, s61
	v_lshl_add_u64 v[48:49], s[26:27], 0, v[148:149]
	s_mov_b32 m0, s36
	s_nop 0
	global_load_lds_dwordx4 v[48:49], off
	v_lshl_add_u64 v[48:49], s[26:27], 0, v[150:151]
	s_add_i32 m0, s36, 0x2000
	s_nop 0
	global_load_lds_dwordx4 v[48:49], off
	s_waitcnt vmcnt(6)
	s_barrier
	s_setprio 1
	v_mfma_f32_16x16x32_bf16 v[60:63], v[242:245], v[196:199], v[60:63]
	v_mfma_f32_16x16x32_bf16 v[56:59], v[234:237], v[204:207], v[56:59]
	v_mfma_f32_16x16x32_bf16 v[52:55], v[242:245], v[204:207], v[52:55]
	v_mfma_f32_16x16x32_bf16 v[32:35], v[234:237], v[218:221], v[32:35]
	v_mfma_f32_16x16x32_bf16 v[28:31], v[242:245], v[218:221], v[28:31]
	v_mfma_f32_16x16x32_bf16 v[24:27], v[234:237], v[226:229], v[24:27]
	v_mfma_f32_16x16x32_bf16 v[20:23], v[242:245], v[226:229], v[20:23]
	v_mfma_f32_16x16x32_bf16 v[48:51], v[234:237], v[196:199], v[64:67]
	v_mfma_f32_16x16x32_bf16 v[60:63], v[246:249], v[200:203], v[60:63]
	v_mfma_f32_16x16x32_bf16 v[56:59], v[238:241], v[214:217], v[56:59]
	v_mfma_f32_16x16x32_bf16 v[52:55], v[246:249], v[214:217], v[52:55]
	v_mfma_f32_16x16x32_bf16 v[32:35], v[238:241], v[222:225], v[32:35]
	v_mfma_f32_16x16x32_bf16 v[28:31], v[246:249], v[222:225], v[28:31]
	v_mfma_f32_16x16x32_bf16 v[24:27], v[238:241], v[230:233], v[24:27]
	v_mfma_f32_16x16x32_bf16 v[20:23], v[246:249], v[230:233], v[20:23]
	v_mfma_f32_16x16x32_bf16 v[48:51], v[238:241], v[200:203], v[48:51]
	s_setprio 0
	s_add_i32 s26, 0, 0x18000
	v_add_u32_e32 v2, s26, v175
	s_barrier
	ds_read_b128 v[64:67], v2
	ds_read_b128 v[184:187], v2 offset:1024
	ds_read_b128 v[188:191], v2 offset:2048
	ds_read_b128 v[192:195], v2 offset:3072
	s_mov_b32 m0, s64
	ds_read_b128 v[196:199], v176 offset:32768
	ds_read_b128 v[200:203], v176 offset:33792
	ds_read_b128 v[204:207], v176 offset:34816
	ds_read_b128 v[214:217], v176 offset:35840
	ds_read_b128 v[218:221], v176 offset:36864
	ds_read_b128 v[222:225], v176 offset:37888
	ds_read_b128 v[226:229], v176 offset:38912
	ds_read_b128 v[230:233], v176 offset:39936
	global_load_lds_dwordx4 v37, s[34:35]
	s_mov_b32 m0, s65
	s_nop 0
	global_load_lds_dwordx4 v39, s[34:35]
	s_waitcnt lgkmcnt(8)
	s_barrier
	s_waitcnt lgkmcnt(0)
	s_setprio 1
	s_waitcnt lgkmcnt(0)
	v_mfma_f32_16x16x32_bf16 v[144:147], v[64:67], v[196:199], v[144:147]
	v_mfma_f32_16x16x32_bf16 v[140:143], v[188:191], v[196:199], v[140:143]
	v_mfma_f32_16x16x32_bf16 v[136:139], v[64:67], v[204:207], v[136:139]
	v_mfma_f32_16x16x32_bf16 v[132:135], v[188:191], v[204:207], v[132:135]
	v_mfma_f32_16x16x32_bf16 v[112:115], v[64:67], v[218:221], v[112:115]
	v_mfma_f32_16x16x32_bf16 v[108:111], v[188:191], v[218:221], v[108:111]
	v_mfma_f32_16x16x32_bf16 v[104:107], v[64:67], v[226:229], v[104:107]
	v_mfma_f32_16x16x32_bf16 v[100:103], v[188:191], v[226:229], v[100:103]
	v_mfma_f32_16x16x32_bf16 v[144:147], v[184:187], v[200:203], v[144:147]
	v_mfma_f32_16x16x32_bf16 v[140:143], v[192:195], v[200:203], v[140:143]
	v_mfma_f32_16x16x32_bf16 v[136:139], v[184:187], v[214:217], v[136:139]
	v_mfma_f32_16x16x32_bf16 v[132:135], v[192:195], v[214:217], v[132:135]
	v_mfma_f32_16x16x32_bf16 v[112:115], v[184:187], v[222:225], v[112:115]
	v_mfma_f32_16x16x32_bf16 v[108:111], v[192:195], v[222:225], v[108:111]
	v_mfma_f32_16x16x32_bf16 v[104:107], v[184:187], v[230:233], v[104:107]
	v_mfma_f32_16x16x32_bf16 v[100:103], v[192:195], v[230:233], v[100:103]
	s_setprio 0
	s_barrier
	s_add_i32 s27, 0, 0x1c000
	s_add_i32 s26, s26, s61
	v_add_u32_e32 v2, s27, v175
	v_lshl_add_u64 v[250:251], v[250:251], 0, s[8:9]
	s_mov_b32 m0, s26
	ds_read_b128 v[234:237], v2
	ds_read_b128 v[238:241], v2 offset:1024
	ds_read_b128 v[242:245], v2 offset:2048
	ds_read_b128 v[246:249], v2 offset:3072
	global_load_lds_dwordx4 v[250:251], off
	v_lshl_add_u64 v[250:251], v[252:253], 0, s[8:9]
	s_add_i32 m0, s26, 0x2000
	s_nop 0
	global_load_lds_dwordx4 v[250:251], off
	s_barrier
	s_waitcnt lgkmcnt(0)
	s_setprio 1
	s_waitcnt lgkmcnt(0)
	v_mfma_f32_16x16x32_bf16 v[128:131], v[234:237], v[196:199], v[128:131]
	v_mfma_f32_16x16x32_bf16 v[124:127], v[242:245], v[196:199], v[124:127]
	v_mfma_f32_16x16x32_bf16 v[120:123], v[234:237], v[204:207], v[120:123]
	v_mfma_f32_16x16x32_bf16 v[116:119], v[242:245], v[204:207], v[116:119]
	v_mfma_f32_16x16x32_bf16 v[96:99], v[234:237], v[218:221], v[96:99]
	v_mfma_f32_16x16x32_bf16 v[92:95], v[242:245], v[218:221], v[92:95]
	v_mfma_f32_16x16x32_bf16 v[88:91], v[234:237], v[226:229], v[88:91]
	v_mfma_f32_16x16x32_bf16 v[84:87], v[242:245], v[226:229], v[84:87]
	v_mfma_f32_16x16x32_bf16 v[128:131], v[238:241], v[200:203], v[128:131]
	v_mfma_f32_16x16x32_bf16 v[124:127], v[246:249], v[200:203], v[124:127]
	v_mfma_f32_16x16x32_bf16 v[120:123], v[238:241], v[214:217], v[120:123]
	v_mfma_f32_16x16x32_bf16 v[116:119], v[246:249], v[214:217], v[116:119]
	v_mfma_f32_16x16x32_bf16 v[96:99], v[238:241], v[222:225], v[96:99]
	v_mfma_f32_16x16x32_bf16 v[92:95], v[246:249], v[222:225], v[92:95]
	v_mfma_f32_16x16x32_bf16 v[88:91], v[238:241], v[230:233], v[88:91]
	v_mfma_f32_16x16x32_bf16 v[84:87], v[246:249], v[230:233], v[84:87]
	s_setprio 0
	s_mov_b32 m0, s72
	v_lshl_add_u64 v[208:209], v[208:209], 0, s[8:9]
	s_barrier
	ds_read_b128 v[196:199], v176 offset:49152
	ds_read_b128 v[200:203], v176 offset:50176
	ds_read_b128 v[204:207], v176 offset:51200
	ds_read_b128 v[214:217], v176 offset:52224
	ds_read_b128 v[218:221], v176 offset:53248
	ds_read_b128 v[222:225], v176 offset:54272
	ds_read_b128 v[226:229], v176 offset:55296
	ds_read_b128 v[230:233], v176 offset:56320
	global_load_lds_dwordx4 v[208:209], off
	v_lshl_add_u64 v[170:171], v[170:171], 0, s[8:9]
	s_mov_b32 m0, s73
	s_nop 0
	global_load_lds_dwordx4 v[170:171], off
	s_barrier
	s_waitcnt lgkmcnt(0)
	s_setprio 1
	s_waitcnt lgkmcnt(0)
	v_mfma_f32_16x16x32_bf16 v[80:83], v[64:67], v[196:199], v[80:83]
	v_mfma_f32_16x16x32_bf16 v[76:79], v[188:191], v[196:199], v[76:79]
	v_mfma_f32_16x16x32_bf16 v[72:75], v[64:67], v[204:207], v[72:75]
	v_mfma_f32_16x16x32_bf16 v[68:71], v[188:191], v[204:207], v[68:71]
	v_mfma_f32_16x16x32_bf16 v[16:19], v[64:67], v[218:221], v[16:19]
	v_mfma_f32_16x16x32_bf16 v[12:15], v[188:191], v[218:221], v[12:15]
	v_mfma_f32_16x16x32_bf16 v[8:11], v[64:67], v[226:229], v[8:11]
	v_mfma_f32_16x16x32_bf16 v[4:7], v[188:191], v[226:229], v[4:7]
	v_mfma_f32_16x16x32_bf16 v[80:83], v[184:187], v[200:203], v[80:83]
	v_mfma_f32_16x16x32_bf16 v[76:79], v[192:195], v[200:203], v[76:79]
	v_mfma_f32_16x16x32_bf16 v[72:75], v[184:187], v[214:217], v[72:75]
	v_mfma_f32_16x16x32_bf16 v[68:71], v[192:195], v[214:217], v[68:71]
	v_mfma_f32_16x16x32_bf16 v[16:19], v[184:187], v[222:225], v[16:19]
	v_mfma_f32_16x16x32_bf16 v[12:15], v[192:195], v[222:225], v[12:15]
	v_mfma_f32_16x16x32_bf16 v[8:11], v[184:187], v[230:233], v[8:11]
	v_mfma_f32_16x16x32_bf16 v[4:7], v[192:195], v[230:233], v[4:7]
	s_setprio 0
	s_barrier
	s_add_u32 s14, s14, 0x40080
	s_addc_u32 s15, s15, 0
	s_add_i32 s26, s27, s61
	v_lshl_add_u64 v[64:65], s[14:15], 0, v[148:149]
	s_mov_b32 m0, s26
	s_nop 0
	global_load_lds_dwordx4 v[64:65], off
	v_lshl_add_u64 v[64:65], s[14:15], 0, v[150:151]
	s_add_i32 m0, s26, 0x2000
	s_nop 0
	global_load_lds_dwordx4 v[64:65], off
	s_waitcnt vmcnt(6)
	s_barrier
	s_setprio 1
	v_mfma_f32_16x16x32_bf16 v[48:51], v[234:237], v[196:199], v[48:51]
	v_mfma_f32_16x16x32_bf16 v[64:67], v[238:241], v[200:203], v[48:51]
	v_mfma_f32_16x16x32_bf16 v[48:51], v[242:245], v[196:199], v[60:63]
	v_mfma_f32_16x16x32_bf16 v[60:63], v[246:249], v[200:203], v[48:51]
	v_mfma_f32_16x16x32_bf16 v[48:51], v[234:237], v[204:207], v[56:59]
	v_mfma_f32_16x16x32_bf16 v[56:59], v[238:241], v[214:217], v[48:51]
	v_mfma_f32_16x16x32_bf16 v[48:51], v[242:245], v[204:207], v[52:55]
	v_mfma_f32_16x16x32_bf16 v[32:35], v[234:237], v[218:221], v[32:35]
	v_mfma_f32_16x16x32_bf16 v[28:31], v[242:245], v[218:221], v[28:31]
	v_mfma_f32_16x16x32_bf16 v[24:27], v[234:237], v[226:229], v[24:27]
	v_mfma_f32_16x16x32_bf16 v[20:23], v[242:245], v[226:229], v[20:23]
	v_mfma_f32_16x16x32_bf16 v[52:55], v[246:249], v[214:217], v[48:51]
	v_mfma_f32_16x16x32_bf16 v[32:35], v[238:241], v[222:225], v[32:35]
	v_mfma_f32_16x16x32_bf16 v[28:31], v[246:249], v[222:225], v[28:31]
	v_mfma_f32_16x16x32_bf16 v[24:27], v[238:241], v[230:233], v[24:27]
	v_mfma_f32_16x16x32_bf16 v[20:23], v[246:249], v[230:233], v[20:23]
	s_setprio 0
	s_add_i32 s25, s25, 2
	s_add_u32 s12, s12, 0x100
	s_addc_u32 s13, s13, 0
	s_cmp_gt_u32 s25, 13
	s_barrier
	s_cbranch_scc0 .LBB0_1324
	s_mul_hi_i32 s0, s2, 0x3e0f83e1
	s_lshr_b32 s1, s0, 31
	s_ashr_i32 s0, s0, 3
	s_add_i32 s0, s0, s1
	s_mul_i32 s1, s0, 33
	s_sub_i32 s1, s2, s1
	s_cmp_lg_u32 s1, 0
	s_cselect_b32 s0, s0, 8
	s_mul_hi_i32 s1, s0, 0x6000
	s_mulk_i32 s0, 0x6000
	s_add_u32 s14, s69, s0
	s_addc_u32 s15, s70, s1
	s_ashr_i32 s3, s2, 31
	s_lshl_b64 s[0:1], s[2:3], 19
	s_lshl_b32 s2, s7, 8
	s_ashr_i32 s3, s2, 31
	s_lshl_b64 s[12:13], s[2:3], 2
	s_add_u32 s7, s14, s12
	s_addc_u32 s13, s15, s13
	s_lshl_b32 s12, s71, 2
	s_add_u32 s12, s7, s12
	s_addc_u32 s13, s13, 0
	v_lshlrev_b32_e32 v2, 2, v152
	v_lshl_add_u64 v[36:37], s[12:13], 0, v[2:3]
	s_mov_b64 s[12:13], 0x6000
	s_movk_i32 s7, 0x6000
	v_lshl_add_u64 v[38:39], v[36:37], 0, s[12:13]
	v_add_co_u32_e32 v36, vcc, s7, v36
	s_add_u32 s7, s66, s0
	s_addc_u32 s12, s67, s1
	s_lshl_b64 s[0:1], s[2:3], 1
	s_add_u32 s0, s7, s0
	s_addc_u32 s1, s12, s1
	s_lshl_b32 s2, s71, 1
	s_add_u32 s0, s0, s2
	s_addc_u32 s1, s1, 0
	v_lshlrev_b32_e32 v2, 1, v152
	v_lshl_add_u64 v[170:171], s[0:1], 0, v[2:3]
	v_lshl_add_u64 v[186:187], v[170:171], 0, v[158:159]
	global_load_dword v188, v[186:187], off
	global_load_dword v188, v[186:187], off offset:256
	v_lshl_add_u64 v[186:187], v[170:171], 0, v[160:161]
	global_load_dword v188, v[186:187], off
	global_load_dword v188, v[186:187], off offset:256
	v_lshl_add_u64 v[186:187], v[170:171], 0, v[162:163]
	global_load_dword v188, v[186:187], off
	global_load_dword v188, v[186:187], off offset:256
	v_lshl_add_u64 v[186:187], v[170:171], 0, v[164:165]
	global_load_dword v188, v[186:187], off
	global_load_dword v188, v[186:187], off offset:256
	v_lshl_add_u64 v[186:187], v[170:171], 0, v[166:167]
	global_load_dword v188, v[186:187], off
	global_load_dword v188, v[186:187], off offset:256
	v_lshl_add_u64 v[186:187], v[170:171], 0, v[168:169]
	global_load_dword v188, v[186:187], off
	global_load_dword v188, v[186:187], off offset:256
	v_addc_co_u32_e32 v37, vcc, 0, v37, vcc
	v_lshl_add_u64 v[184:185], v[170:171], 0, v[154:155]
	global_load_dwordx4 v[48:51], v[36:37], off
	global_load_dwordx4 v[44:47], v[38:39], off offset:64
	global_load_dwordx4 v[40:43], v[38:39], off offset:512
	s_nop 0
	global_load_dwordx4 v[36:39], v[38:39], off offset:576
	v_lshl_add_u64 v[202:203], v[170:171], 0, v[156:157]
	global_load_dwordx2 v[186:187], v[184:185], off
	global_load_dwordx2 v[190:191], v[184:185], off offset:32
	global_load_dwordx2 v[194:195], v[184:185], off offset:256
	global_load_dwordx2 v[198:199], v[184:185], off offset:288
	global_load_dwordx2 v[204:205], v[202:203], off
	global_load_dwordx2 v[214:215], v[202:203], off offset:32
	global_load_dwordx2 v[218:219], v[202:203], off offset:256
	global_load_dwordx2 v[222:223], v[202:203], off offset:288
	s_and_b64 vcc, exec, s[38:39]
	s_mov_b32 s7, s52
	s_mov_b32 s2, s76
	s_mov_b64 s[12:13], s[54:55]
	s_movk_i32 s36, 0x1ff
	s_waitcnt vmcnt(0)
	v_lshlrev_b32_e32 v188, 16, v186
	v_and_b32_e32 v189, 0xffff0000, v186
	v_lshlrev_b32_e32 v196, 16, v194
	v_lshlrev_b32_e32 v200, 16, v198
	v_and_b32_e32 v201, 0xffff0000, v198
	v_lshlrev_b32_e32 v198, 16, v199
	v_and_b32_e32 v199, 0xffff0000, v199
	v_pk_fma_f32 v[126:127], v[126:127], v[38:39], v[198:199]
	v_pk_fma_f32 v[124:125], v[124:125], v[36:37], v[200:201]
	v_lshlrev_b32_e32 v206, 16, v204
	v_and_b32_e32 v207, 0xffff0000, v204
	v_lshlrev_b32_e32 v204, 16, v205
	v_and_b32_e32 v205, 0xffff0000, v205
	v_cvt_pk_bf16_f32 v124, v124, v125
	v_cvt_pk_bf16_f32 v125, v126, v127
	v_lshlrev_b32_e32 v224, 16, v222
	v_and_b32_e32 v225, 0xffff0000, v222
	v_lshlrev_b32_e32 v222, 16, v223
	v_and_b32_e32 v223, 0xffff0000, v223
	global_store_dwordx2 v[184:185], v[124:125], off offset:288
	v_pk_fma_f32 v[124:125], v[138:139], v[50:51], v[204:205]
	v_pk_fma_f32 v[126:127], v[136:137], v[48:49], v[206:207]
	v_lshlrev_b32_e32 v216, 16, v214
	v_and_b32_e32 v217, 0xffff0000, v214
	v_lshlrev_b32_e32 v214, 16, v215
	v_and_b32_e32 v215, 0xffff0000, v215
	v_cvt_pk_bf16_f32 v126, v126, v127
	v_cvt_pk_bf16_f32 v127, v124, v125
	v_pk_fma_f32 v[118:119], v[118:119], v[38:39], v[222:223]
	v_pk_fma_f32 v[116:117], v[116:117], v[36:37], v[224:225]
	v_and_b32_e32 v197, 0xffff0000, v194
	v_lshlrev_b32_e32 v194, 16, v195
	v_and_b32_e32 v195, 0xffff0000, v195
	v_lshlrev_b32_e32 v220, 16, v218
	v_and_b32_e32 v221, 0xffff0000, v218
	v_lshlrev_b32_e32 v218, 16, v219
	v_and_b32_e32 v219, 0xffff0000, v219
	global_store_dwordx2 v[202:203], v[126:127], off
	v_pk_fma_f32 v[124:125], v[134:135], v[46:47], v[214:215]
	v_pk_fma_f32 v[126:127], v[132:133], v[44:45], v[216:217]
	v_cvt_pk_bf16_f32 v116, v116, v117
	v_cvt_pk_bf16_f32 v117, v118, v119
	v_pk_fma_f32 v[130:131], v[130:131], v[42:43], v[194:195]
	v_pk_fma_f32 v[128:129], v[128:129], v[40:41], v[196:197]
	v_cvt_pk_bf16_f32 v126, v126, v127
	v_cvt_pk_bf16_f32 v127, v124, v125
	v_pk_fma_f32 v[122:123], v[122:123], v[42:43], v[218:219]
	v_pk_fma_f32 v[120:121], v[120:121], v[40:41], v[220:221]
	global_store_dwordx2 v[202:203], v[116:117], off offset:288
	v_lshl_add_u64 v[116:117], v[170:171], 0, v[158:159]
	v_lshlrev_b32_e32 v186, 16, v187
	v_and_b32_e32 v187, 0xffff0000, v187
	v_lshlrev_b32_e32 v192, 16, v190
	v_and_b32_e32 v193, 0xffff0000, v190
	v_lshlrev_b32_e32 v190, 16, v191
	v_and_b32_e32 v191, 0xffff0000, v191
	v_cvt_pk_bf16_f32 v128, v128, v129
	v_cvt_pk_bf16_f32 v129, v130, v131
	global_store_dwordx2 v[202:203], v[126:127], off offset:32
	v_cvt_pk_bf16_f32 v120, v120, v121
	v_cvt_pk_bf16_f32 v121, v122, v123
	global_load_dwordx2 v[118:119], v[116:117], off
	global_load_dwordx2 v[122:123], v[116:117], off offset:32
	global_load_dwordx2 v[126:127], v[116:117], off offset:256
	global_load_dwordx2 v[130:131], v[116:117], off offset:288
	v_pk_fma_f32 v[146:147], v[146:147], v[50:51], v[186:187]
	v_pk_fma_f32 v[144:145], v[144:145], v[48:49], v[188:189]
	v_pk_fma_f32 v[142:143], v[142:143], v[46:47], v[190:191]
	v_pk_fma_f32 v[140:141], v[140:141], v[44:45], v[192:193]
	v_lshl_add_u64 v[134:135], v[170:171], 0, v[160:161]
	v_cvt_pk_bf16_f32 v144, v144, v145
	v_cvt_pk_bf16_f32 v145, v146, v147
	v_cvt_pk_bf16_f32 v140, v140, v141
	v_cvt_pk_bf16_f32 v141, v142, v143
	global_load_dwordx2 v[136:137], v[134:135], off
	s_waitcnt vmcnt(0)
	v_lshlrev_b32_e32 v124, 16, v122
	global_store_dwordx2 v[184:185], v[144:145], off
	global_store_dwordx2 v[184:185], v[140:141], off offset:32
	global_store_dwordx2 v[184:185], v[128:129], off offset:256
	global_load_dwordx2 v[140:141], v[134:135], off offset:32
	v_lshlrev_b32_e32 v132, 16, v130
	global_load_dwordx2 v[144:145], v[134:135], off offset:256
	global_load_dwordx2 v[184:185], v[134:135], off offset:288
	v_and_b32_e32 v133, 0xffff0000, v130
	v_lshlrev_b32_e32 v130, 16, v131
	v_and_b32_e32 v131, 0xffff0000, v131
	v_pk_fma_f32 v[94:95], v[94:95], v[38:39], v[130:131]
	v_pk_fma_f32 v[92:93], v[92:93], v[36:37], v[132:133]
	v_lshlrev_b32_e32 v138, 16, v136
	v_and_b32_e32 v139, 0xffff0000, v136
	v_lshlrev_b32_e32 v136, 16, v137
	v_and_b32_e32 v137, 0xffff0000, v137
	v_cvt_pk_bf16_f32 v92, v92, v93
	v_cvt_pk_bf16_f32 v93, v94, v95
	global_store_dwordx2 v[116:117], v[92:93], off offset:288
	v_pk_fma_f32 v[92:93], v[106:107], v[50:51], v[136:137]
	v_pk_fma_f32 v[94:95], v[104:105], v[48:49], v[138:139]
	v_lshlrev_b32_e32 v128, 16, v126
	v_cvt_pk_bf16_f32 v94, v94, v95
	v_cvt_pk_bf16_f32 v95, v92, v93
	v_and_b32_e32 v129, 0xffff0000, v126
	v_lshlrev_b32_e32 v126, 16, v127
	v_and_b32_e32 v127, 0xffff0000, v127
	global_store_dwordx2 v[134:135], v[94:95], off
	v_pk_fma_f32 v[98:99], v[98:99], v[42:43], v[126:127]
	v_pk_fma_f32 v[96:97], v[96:97], v[40:41], v[128:129]
	global_store_dwordx2 v[202:203], v[120:121], off offset:256
	v_lshlrev_b32_e32 v120, 16, v118
	v_and_b32_e32 v121, 0xffff0000, v118
	v_lshlrev_b32_e32 v118, 16, v119
	v_and_b32_e32 v119, 0xffff0000, v119
	v_and_b32_e32 v125, 0xffff0000, v122
	v_lshlrev_b32_e32 v122, 16, v123
	v_and_b32_e32 v123, 0xffff0000, v123
	v_cvt_pk_bf16_f32 v96, v96, v97
	v_cvt_pk_bf16_f32 v97, v98, v99
	v_pk_fma_f32 v[114:115], v[114:115], v[50:51], v[118:119]
	v_pk_fma_f32 v[112:113], v[112:113], v[48:49], v[120:121]
	v_pk_fma_f32 v[110:111], v[110:111], v[46:47], v[122:123]
	v_pk_fma_f32 v[108:109], v[108:109], v[44:45], v[124:125]
	v_cvt_pk_bf16_f32 v112, v112, v113
	v_cvt_pk_bf16_f32 v113, v114, v115
	v_cvt_pk_bf16_f32 v108, v108, v109
	v_cvt_pk_bf16_f32 v109, v110, v111
	global_store_dwordx2 v[116:117], v[112:113], off
	global_store_dwordx2 v[116:117], v[108:109], off offset:32
	global_store_dwordx2 v[116:117], v[96:97], off offset:256
	s_waitcnt vmcnt(0)
	v_lshlrev_b32_e32 v142, 16, v140
	v_and_b32_e32 v143, 0xffff0000, v140
	v_lshlrev_b32_e32 v140, 16, v141
	v_lshlrev_b32_e32 v186, 16, v184
	v_and_b32_e32 v187, 0xffff0000, v184
	v_lshlrev_b32_e32 v184, 16, v185
	v_and_b32_e32 v185, 0xffff0000, v185
	v_and_b32_e32 v141, 0xffff0000, v141
	v_pk_fma_f32 v[86:87], v[86:87], v[38:39], v[184:185]
	v_pk_fma_f32 v[84:85], v[84:85], v[36:37], v[186:187]
	v_lshlrev_b32_e32 v146, 16, v144
	v_and_b32_e32 v147, 0xffff0000, v144
	v_lshlrev_b32_e32 v144, 16, v145
	v_and_b32_e32 v145, 0xffff0000, v145
	v_pk_fma_f32 v[92:93], v[102:103], v[46:47], v[140:141]
	v_pk_fma_f32 v[94:95], v[100:101], v[44:45], v[142:143]
	v_cvt_pk_bf16_f32 v84, v84, v85
	v_cvt_pk_bf16_f32 v85, v86, v87
	v_cvt_pk_bf16_f32 v94, v94, v95
	v_cvt_pk_bf16_f32 v95, v92, v93
	v_pk_fma_f32 v[90:91], v[90:91], v[42:43], v[144:145]
	v_pk_fma_f32 v[88:89], v[88:89], v[40:41], v[146:147]
	global_store_dwordx2 v[134:135], v[84:85], off offset:288
	v_lshl_add_u64 v[84:85], v[170:171], 0, v[162:163]
	global_store_dwordx2 v[134:135], v[94:95], off offset:32
	v_cvt_pk_bf16_f32 v88, v88, v89
	v_cvt_pk_bf16_f32 v89, v90, v91
	global_load_dwordx2 v[90:91], v[84:85], off offset:32
	global_load_dwordx2 v[94:95], v[84:85], off offset:256
	global_load_dwordx2 v[98:99], v[84:85], off offset:288
	v_lshl_add_u64 v[102:103], v[170:171], 0, v[164:165]
	global_load_dwordx2 v[104:105], v[102:103], off
	global_load_dwordx2 v[108:109], v[102:103], off offset:32
	global_load_dwordx2 v[112:113], v[102:103], off offset:256
	global_load_dwordx2 v[116:117], v[102:103], off offset:288
	s_waitcnt vmcnt(0)
	v_lshlrev_b32_e32 v96, 16, v94
	v_lshlrev_b32_e32 v100, 16, v98
	v_and_b32_e32 v101, 0xffff0000, v98
	v_lshlrev_b32_e32 v98, 16, v99
	v_and_b32_e32 v99, 0xffff0000, v99
	v_pk_fma_f32 v[62:63], v[62:63], v[38:39], v[98:99]
	v_pk_fma_f32 v[60:61], v[60:61], v[36:37], v[100:101]
	v_lshlrev_b32_e32 v106, 16, v104
	v_and_b32_e32 v107, 0xffff0000, v104
	v_lshlrev_b32_e32 v104, 16, v105
	v_and_b32_e32 v105, 0xffff0000, v105
	v_cvt_pk_bf16_f32 v60, v60, v61
	v_cvt_pk_bf16_f32 v61, v62, v63
	v_lshlrev_b32_e32 v118, 16, v116
	v_and_b32_e32 v119, 0xffff0000, v116
	v_lshlrev_b32_e32 v116, 16, v117
	v_and_b32_e32 v117, 0xffff0000, v117
	global_store_dwordx2 v[84:85], v[60:61], off offset:288
	v_pk_fma_f32 v[60:61], v[74:75], v[50:51], v[104:105]
	v_pk_fma_f32 v[62:63], v[72:73], v[48:49], v[106:107]
	v_lshlrev_b32_e32 v110, 16, v108
	v_and_b32_e32 v111, 0xffff0000, v108
	v_lshlrev_b32_e32 v108, 16, v109
	v_and_b32_e32 v109, 0xffff0000, v109
	v_lshlrev_b32_e32 v114, 16, v112
	v_and_b32_e32 v115, 0xffff0000, v112
	v_lshlrev_b32_e32 v112, 16, v113
	v_and_b32_e32 v113, 0xffff0000, v113
	v_cvt_pk_bf16_f32 v62, v62, v63
	v_cvt_pk_bf16_f32 v63, v60, v61
	v_pk_fma_f32 v[54:55], v[54:55], v[38:39], v[116:117]
	v_pk_fma_f32 v[52:53], v[52:53], v[36:37], v[118:119]
	global_store_dwordx2 v[102:103], v[62:63], off
	v_pk_fma_f32 v[60:61], v[70:71], v[46:47], v[108:109]
	v_pk_fma_f32 v[62:63], v[68:69], v[44:45], v[110:111]
	v_pk_fma_f32 v[58:59], v[58:59], v[42:43], v[112:113]
	v_pk_fma_f32 v[56:57], v[56:57], v[40:41], v[114:115]
	v_cvt_pk_bf16_f32 v52, v52, v53
	v_cvt_pk_bf16_f32 v53, v54, v55
	v_cvt_pk_bf16_f32 v62, v62, v63
	v_cvt_pk_bf16_f32 v63, v60, v61
	v_cvt_pk_bf16_f32 v56, v56, v57
	v_cvt_pk_bf16_f32 v57, v58, v59
	global_store_dwordx2 v[102:103], v[52:53], off offset:288
	v_lshl_add_u64 v[52:53], v[170:171], 0, v[166:167]
	global_store_dwordx2 v[134:135], v[88:89], off offset:256
	global_load_dwordx2 v[88:89], v[84:85], off
	v_and_b32_e32 v97, 0xffff0000, v94
	global_store_dwordx2 v[102:103], v[62:63], off offset:32
	global_store_dwordx2 v[102:103], v[56:57], off offset:256
	global_load_dwordx2 v[56:57], v[52:53], off
	v_lshlrev_b32_e32 v94, 16, v95
	global_load_dwordx2 v[60:61], v[52:53], off offset:32
	global_load_dwordx2 v[62:63], v[52:53], off offset:256
	v_and_b32_e32 v95, 0xffff0000, v95
	v_pk_fma_f32 v[66:67], v[66:67], v[42:43], v[94:95]
	v_pk_fma_f32 v[64:65], v[64:65], v[40:41], v[96:97]
	s_waitcnt vmcnt(0)
	v_lshlrev_b32_e32 v86, 16, v88
	v_cvt_pk_bf16_f32 v64, v64, v65
	v_cvt_pk_bf16_f32 v65, v66, v67
	global_store_dwordx2 v[84:85], v[64:65], off offset:256
	v_and_b32_e32 v87, 0xffff0000, v88
	v_lshlrev_b32_e32 v88, 16, v89
	v_and_b32_e32 v89, 0xffff0000, v89
	v_lshlrev_b32_e32 v64, 16, v62
	v_and_b32_e32 v65, 0xffff0000, v62
	v_lshlrev_b32_e32 v66, 16, v63
	v_and_b32_e32 v67, 0xffff0000, v63
	global_load_dwordx2 v[62:63], v[52:53], off offset:288
	v_lshlrev_b32_e32 v92, 16, v90
	v_and_b32_e32 v93, 0xffff0000, v90
	v_lshlrev_b32_e32 v90, 16, v91
	v_and_b32_e32 v91, 0xffff0000, v91
	v_pk_fma_f32 v[78:79], v[78:79], v[46:47], v[90:91]
	v_pk_fma_f32 v[76:77], v[76:77], v[44:45], v[92:93]
	v_pk_fma_f32 v[82:83], v[82:83], v[50:51], v[88:89]
	v_cvt_pk_bf16_f32 v76, v76, v77
	v_cvt_pk_bf16_f32 v77, v78, v79
	v_pk_fma_f32 v[80:81], v[80:81], v[48:49], v[86:87]
	global_store_dwordx2 v[84:85], v[76:77], off offset:32
	v_cvt_pk_bf16_f32 v80, v80, v81
	v_cvt_pk_bf16_f32 v81, v82, v83
	global_store_dwordx2 v[84:85], v[80:81], off
	v_lshlrev_b32_e32 v58, 16, v60
	v_and_b32_e32 v59, 0xffff0000, v60
	v_lshlrev_b32_e32 v60, 16, v61
	v_and_b32_e32 v61, 0xffff0000, v61
	v_pk_fma_f32 v[14:15], v[14:15], v[46:47], v[60:61]
	v_pk_fma_f32 v[12:13], v[12:13], v[44:45], v[58:59]
	v_lshlrev_b32_e32 v54, 16, v56
	v_cvt_pk_bf16_f32 v12, v12, v13
	v_cvt_pk_bf16_f32 v13, v14, v15
	global_store_dwordx2 v[52:53], v[12:13], off offset:32
	v_pk_fma_f32 v[12:13], v[34:35], v[42:43], v[66:67]
	v_pk_fma_f32 v[14:15], v[32:33], v[40:41], v[64:65]
	v_and_b32_e32 v55, 0xffff0000, v56
	v_lshlrev_b32_e32 v56, 16, v57
	v_and_b32_e32 v57, 0xffff0000, v57
	v_cvt_pk_bf16_f32 v14, v14, v15
	v_cvt_pk_bf16_f32 v15, v12, v13
	v_pk_fma_f32 v[18:19], v[18:19], v[50:51], v[56:57]
	v_pk_fma_f32 v[16:17], v[16:17], v[48:49], v[54:55]
	global_store_dwordx2 v[52:53], v[14:15], off offset:256
	v_cvt_pk_bf16_f32 v16, v16, v17
	v_cvt_pk_bf16_f32 v17, v18, v19
	global_store_dwordx2 v[52:53], v[16:17], off
	s_waitcnt vmcnt(0)
	v_lshlrev_b32_e32 v68, 16, v62
	v_and_b32_e32 v69, 0xffff0000, v62
	v_lshlrev_b32_e32 v70, 16, v63
	v_and_b32_e32 v71, 0xffff0000, v63
	v_lshl_add_u64 v[62:63], v[170:171], 0, v[168:169]
	global_load_dwordx2 v[74:75], v[62:63], off
	global_load_dwordx2 v[78:79], v[62:63], off offset:32
	global_load_dwordx2 v[82:83], v[62:63], off offset:256
	global_load_dwordx2 v[84:85], v[62:63], off offset:288
	v_pk_fma_f32 v[12:13], v[30:31], v[38:39], v[70:71]
	v_pk_fma_f32 v[14:15], v[28:29], v[36:37], v[68:69]
	s_waitcnt vmcnt(0)
	v_lshlrev_b32_e32 v72, 16, v74
	v_lshlrev_b32_e32 v76, 16, v78
	v_and_b32_e32 v77, 0xffff0000, v78
	v_lshlrev_b32_e32 v78, 16, v79
	v_and_b32_e32 v79, 0xffff0000, v79
	v_pk_fma_f32 v[6:7], v[6:7], v[46:47], v[78:79]
	v_pk_fma_f32 v[4:5], v[4:5], v[44:45], v[76:77]
	v_lshlrev_b32_e32 v80, 16, v82
	v_and_b32_e32 v81, 0xffff0000, v82
	v_lshlrev_b32_e32 v82, 16, v83
	v_and_b32_e32 v83, 0xffff0000, v83
	v_cvt_pk_bf16_f32 v4, v4, v5
	v_cvt_pk_bf16_f32 v5, v6, v7
	global_store_dwordx2 v[62:63], v[4:5], off offset:32
	v_pk_fma_f32 v[4:5], v[26:27], v[42:43], v[82:83]
	v_pk_fma_f32 v[6:7], v[24:25], v[40:41], v[80:81]
	v_and_b32_e32 v73, 0xffff0000, v74
	v_lshlrev_b32_e32 v74, 16, v75
	v_and_b32_e32 v75, 0xffff0000, v75
	v_lshlrev_b32_e32 v86, 16, v84
	v_and_b32_e32 v87, 0xffff0000, v84
	v_lshlrev_b32_e32 v84, 16, v85
	v_and_b32_e32 v85, 0xffff0000, v85
	v_cvt_pk_bf16_f32 v6, v6, v7
	v_cvt_pk_bf16_f32 v7, v4, v5
	v_pk_fma_f32 v[10:11], v[10:11], v[50:51], v[74:75]
	v_pk_fma_f32 v[8:9], v[8:9], v[48:49], v[72:73]
	global_store_dwordx2 v[62:63], v[6:7], off offset:256
	v_pk_fma_f32 v[4:5], v[22:23], v[38:39], v[84:85]
	v_pk_fma_f32 v[6:7], v[20:21], v[36:37], v[86:87]
	v_cvt_pk_bf16_f32 v14, v14, v15
	v_cvt_pk_bf16_f32 v15, v12, v13
	v_cvt_pk_bf16_f32 v8, v8, v9
	v_cvt_pk_bf16_f32 v9, v10, v11
	v_cvt_pk_bf16_f32 v6, v6, v7
	v_cvt_pk_bf16_f32 v7, v4, v5
	v_mov_b32_e32 v42, v182
	v_mov_b32_e32 v40, v179
	v_mov_b32_e32 v38, v178
	v_mov_b32_e32 v36, v177
	global_store_dwordx2 v[52:53], v[14:15], off offset:288
	global_store_dwordx2 v[62:63], v[8:9], off
	global_store_dwordx2 v[62:63], v[6:7], off offset:288
	s_cbranch_vccz .LBB0_1317
	s_waitcnt vmcnt(0)
	s_cmpk_gt_u32 s23, 0xff
	s_cbranch_scc1 .LBB0_1328
	s_barrier
